# P14 A-operand (hidden activation) LDS-DMA loads nt
# baseline (speedup 1.0000x reference)
.LBB0_1458:
	s_ashr_i32 s41, s40, 31
	s_lshl_b64 s[4:5], s[40:41], 21
	s_add_u32 s42, s6, s4
	s_addc_u32 s43, s7, s5
	s_and_b64 s[4:5], s[38:39], exec
	s_cselect_b32 s41, s43, s49
	s_cselect_b32 s68, s42, s48
	s_ashr_i32 s37, s36, 31
	s_lshl_b64 s[4:5], s[36:37], 21
	s_add_u32 s44, s8, s4
	s_addc_u32 s45, s9, s5
	s_and_b64 s[4:5], s[38:39], exec
	s_cselect_b32 s37, s45, s51
	s_cselect_b32 s69, s44, s50
	s_add_u32 s70, s68, 0x80
	s_addc_u32 s71, s41, 0
	s_add_u32 s72, s50, 0x100
	s_addc_u32 s73, s51, 0
	s_add_u32 s4, s48, 0x100080
	s_addc_u32 s5, s49, 0
	v_lshl_add_u64 v[112:113], s[4:5], 0, v[210:211]
	v_lshl_add_u64 v[114:115], s[4:5], 0, v[212:213]
	s_mov_b32 s74, -2
	s_mov_b64 s[50:51], 0
	s_waitcnt lgkmcnt(0)
	s_waitcnt vmcnt(0)
	s_add_u32 s4, s48, s50
	s_addc_u32 s5, s49, s51
	s_add_u32 s75, s4, 0x100
	s_addc_u32 s76, s5, 0
	s_add_u32 s52, s72, s50
	s_addc_u32 s53, s73, s51
	s_add_u32 s4, s4, 0x180
	s_addc_u32 s5, s5, 0
	s_add_i32 s77, 0, 0x10000
	s_add_i32 s78, 0, 0x14000
	v_add_u32_e32 v148, s77, v203
	v_add_u32_e32 v164, s78, v203
	ds_read_b128 v[120:123], v148
	ds_read_b128 v[132:135], v148 offset:1024
	ds_read_b128 v[144:147], v148 offset:2048
	ds_read_b128 v[148:151], v148 offset:3072
	ds_read_b128 v[152:155], v164
	ds_read_b128 v[156:159], v164 offset:1024
	ds_read_b128 v[160:163], v164 offset:2048
	ds_read_b128 v[164:167], v164 offset:3072
	s_cmpk_eq_i32 s50, 0x1f00
	s_cselect_b32 s13, s71, s5
	s_cselect_b32 s12, s70, s4
	s_cselect_b32 s53, s37, s53
	s_cselect_b32 s52, s69, s52
	s_cselect_b32 s5, s41, s76
	s_cselect_b32 s4, s68, s75
	v_lshl_add_u64 v[214:215], v[112:113], 0, s[50:51]
	s_add_i32 m0, s17, 0xc000
	ds_read_b128 v[168:171], v233
	ds_read_b128 v[172:175], v233 offset:1024
	ds_read_b128 v[176:179], v233 offset:2048
	ds_read_b128 v[180:183], v233 offset:3072
	ds_read_b128 v[184:187], v233 offset:4096
	ds_read_b128 v[188:191], v233 offset:5120
	ds_read_b128 v[192:195], v233 offset:6144
	ds_read_b128 v[196:199], v233 offset:7168
	global_load_lds_dwordx4 v[214:215], off nt
	v_lshl_add_u64 v[214:215], v[114:115], 0, s[50:51]
	s_add_i32 m0, s17, 0xe000
	s_nop 0
	global_load_lds_dwordx4 v[214:215], off nt
	s_waitcnt vmcnt(8)
	s_waitcnt lgkmcnt(0)
	s_barrier
	s_setprio 1
	v_mfma_f32_16x16x32_bf16 v[140:143], v[120:123], v[168:171], 0
	v_mfma_f32_16x16x32_bf16 v[136:139], v[144:147], v[168:171], 0
	v_mfma_f32_16x16x32_bf16 v[116:119], v[120:123], v[176:179], 0
	v_mfma_f32_16x16x32_bf16 v[108:111], v[144:147], v[176:179], 0
	v_mfma_f32_16x16x32_bf16 v[96:99], v[120:123], v[184:187], 0
	v_mfma_f32_16x16x32_bf16 v[92:95], v[144:147], v[184:187], 0
	v_mfma_f32_16x16x32_bf16 v[80:83], v[120:123], v[192:195], 0
	v_mfma_f32_16x16x32_bf16 v[76:79], v[144:147], v[192:195], 0
	v_mfma_f32_16x16x32_bf16 v[140:143], v[132:135], v[172:175], v[140:143]
	v_mfma_f32_16x16x32_bf16 v[136:139], v[148:151], v[172:175], v[136:139]
	v_mfma_f32_16x16x32_bf16 v[116:119], v[132:135], v[180:183], v[116:119]
	v_mfma_f32_16x16x32_bf16 v[108:111], v[148:151], v[180:183], v[108:111]
	v_mfma_f32_16x16x32_bf16 v[96:99], v[132:135], v[188:191], v[96:99]
	v_mfma_f32_16x16x32_bf16 v[92:95], v[148:151], v[188:191], v[92:95]
	v_mfma_f32_16x16x32_bf16 v[80:83], v[132:135], v[196:199], v[80:83]
	v_mfma_f32_16x16x32_bf16 v[76:79], v[148:151], v[196:199], v[76:79]
	v_mfma_f32_16x16x32_bf16 v[128:131], v[152:155], v[168:171], 0
	v_mfma_f32_16x16x32_bf16 v[124:127], v[160:163], v[168:171], 0
	v_mfma_f32_16x16x32_bf16 v[104:107], v[152:155], v[176:179], 0
	v_mfma_f32_16x16x32_bf16 v[100:103], v[160:163], v[176:179], 0
	v_mfma_f32_16x16x32_bf16 v[88:91], v[152:155], v[184:187], 0
	v_mfma_f32_16x16x32_bf16 v[84:87], v[160:163], v[184:187], 0
	v_mfma_f32_16x16x32_bf16 v[72:75], v[152:155], v[192:195], 0
	v_mfma_f32_16x16x32_bf16 v[68:71], v[160:163], v[192:195], 0
	v_mfma_f32_16x16x32_bf16 v[128:131], v[156:159], v[172:175], v[128:131]
	v_mfma_f32_16x16x32_bf16 v[124:127], v[164:167], v[172:175], v[124:127]
	v_mfma_f32_16x16x32_bf16 v[104:107], v[156:159], v[180:183], v[104:107]
	v_mfma_f32_16x16x32_bf16 v[100:103], v[164:167], v[180:183], v[100:103]
	v_mfma_f32_16x16x32_bf16 v[88:91], v[156:159], v[188:191], v[88:91]
	v_mfma_f32_16x16x32_bf16 v[84:87], v[164:167], v[188:191], v[84:87]
	v_mfma_f32_16x16x32_bf16 v[72:75], v[156:159], v[196:199], v[72:75]
	v_mfma_f32_16x16x32_bf16 v[68:71], v[164:167], v[196:199], v[68:71]
	s_setprio 0
	s_barrier
	s_add_i32 s75, s77, s16
	v_lshl_add_u64 v[214:215], s[52:53], 0, v[2:3]
	s_mov_b32 m0, s75
	ds_read_b128 v[168:171], v233 offset:16384
	ds_read_b128 v[172:175], v233 offset:17408
	ds_read_b128 v[176:179], v233 offset:18432
	ds_read_b128 v[180:183], v233 offset:19456
	ds_read_b128 v[184:187], v233 offset:20480
	ds_read_b128 v[188:191], v233 offset:21504
	ds_read_b128 v[192:195], v233 offset:22528
	ds_read_b128 v[196:199], v233 offset:23552
	global_load_lds_dwordx4 v[214:215], off
	s_add_i32 m0, s75, 0x2000
	s_add_u32 s76, s52, 0x100000
	v_lshl_add_u64 v[216:217], s[52:53], 0, v[204:205]
	s_addc_u32 s77, s53, 0
	s_add_i32 s75, s78, s16
	global_load_lds_dwordx4 v[216:217], off
	v_lshl_add_u64 v[218:219], s[76:77], 0, v[2:3]
	s_mov_b32 m0, s75
	s_nop 0
	global_load_lds_dwordx4 v[218:219], off
	v_lshl_add_u64 v[218:219], s[76:77], 0, v[204:205]
	s_add_i32 m0, s75, 0x2000
	s_nop 0
	global_load_lds_dwordx4 v[218:219], off
	v_lshl_add_u64 v[218:219], s[4:5], 0, v[208:209]
	s_mov_b32 m0, s17
	s_nop 0
	global_load_lds_dwordx4 v[218:219], off nt
	v_lshl_add_u64 v[218:219], s[4:5], 0, v[206:207]
	s_mov_b32 m0, s46
	s_nop 0
	global_load_lds_dwordx4 v[218:219], off nt
	s_waitcnt vmcnt(8)
	s_waitcnt lgkmcnt(0)
	s_barrier
	s_setprio 1
	v_mfma_f32_16x16x32_bf16 v[64:67], v[120:123], v[168:171], 0
	v_mfma_f32_16x16x32_bf16 v[60:63], v[144:147], v[168:171], 0
	v_mfma_f32_16x16x32_bf16 v[48:51], v[120:123], v[176:179], 0
	v_mfma_f32_16x16x32_bf16 v[44:47], v[144:147], v[176:179], 0
	v_mfma_f32_16x16x32_bf16 v[32:35], v[120:123], v[184:187], 0
	v_mfma_f32_16x16x32_bf16 v[28:31], v[144:147], v[184:187], 0
	v_mfma_f32_16x16x32_bf16 v[16:19], v[120:123], v[192:195], 0
	v_mfma_f32_16x16x32_bf16 v[12:15], v[144:147], v[192:195], 0
	v_mfma_f32_16x16x32_bf16 v[64:67], v[132:135], v[172:175], v[64:67]
	v_mfma_f32_16x16x32_bf16 v[60:63], v[148:151], v[172:175], v[60:63]
	v_mfma_f32_16x16x32_bf16 v[48:51], v[132:135], v[180:183], v[48:51]
	v_mfma_f32_16x16x32_bf16 v[44:47], v[148:151], v[180:183], v[44:47]
	v_mfma_f32_16x16x32_bf16 v[32:35], v[132:135], v[188:191], v[32:35]
	v_mfma_f32_16x16x32_bf16 v[28:31], v[148:151], v[188:191], v[28:31]
	v_mfma_f32_16x16x32_bf16 v[16:19], v[132:135], v[196:199], v[16:19]
	v_mfma_f32_16x16x32_bf16 v[12:15], v[148:151], v[196:199], v[12:15]
	v_mfma_f32_16x16x32_bf16 v[56:59], v[152:155], v[168:171], 0
	v_mfma_f32_16x16x32_bf16 v[52:55], v[160:163], v[168:171], 0
	v_mfma_f32_16x16x32_bf16 v[40:43], v[152:155], v[176:179], 0
	v_mfma_f32_16x16x32_bf16 v[36:39], v[160:163], v[176:179], 0
	v_mfma_f32_16x16x32_bf16 v[24:27], v[152:155], v[184:187], 0
	v_mfma_f32_16x16x32_bf16 v[20:23], v[160:163], v[184:187], 0
	v_mfma_f32_16x16x32_bf16 v[8:11], v[152:155], v[192:195], 0
	v_mfma_f32_16x16x32_bf16 v[4:7], v[160:163], v[192:195], 0
	v_mfma_f32_16x16x32_bf16 v[56:59], v[156:159], v[172:175], v[56:59]
	v_mfma_f32_16x16x32_bf16 v[52:55], v[164:167], v[172:175], v[52:55]
	v_mfma_f32_16x16x32_bf16 v[40:43], v[156:159], v[180:183], v[40:43]
	v_mfma_f32_16x16x32_bf16 v[36:39], v[164:167], v[180:183], v[36:39]
	v_mfma_f32_16x16x32_bf16 v[24:27], v[156:159], v[188:191], v[24:27]
	v_mfma_f32_16x16x32_bf16 v[20:23], v[164:167], v[188:191], v[20:23]
	v_mfma_f32_16x16x32_bf16 v[8:11], v[156:159], v[196:199], v[8:11]
	v_mfma_f32_16x16x32_bf16 v[4:7], v[164:167], v[196:199], v[4:7]
	s_setprio 0
	s_barrier
	s_add_i32 s75, 0, 0x18000
	s_add_i32 s76, 0, 0x1c000
	v_add_u32_e32 v148, s75, v203
	v_add_u32_e32 v164, s76, v203
	ds_read_b128 v[120:123], v148
	ds_read_b128 v[132:135], v148 offset:1024
	ds_read_b128 v[144:147], v148 offset:2048
	ds_read_b128 v[148:151], v148 offset:3072
	ds_read_b128 v[152:155], v164
	ds_read_b128 v[156:159], v164 offset:1024
	ds_read_b128 v[160:163], v164 offset:2048
	ds_read_b128 v[164:167], v164 offset:3072
	s_add_u32 s4, s4, 0x100000
	s_addc_u32 s5, s5, 0
	s_mov_b32 m0, s47
	v_lshl_add_u64 v[218:219], s[4:5], 0, v[208:209]
	ds_read_b128 v[168:171], v233 offset:32768
	ds_read_b128 v[172:175], v233 offset:33792
	ds_read_b128 v[176:179], v233 offset:34816
	ds_read_b128 v[180:183], v233 offset:35840
	ds_read_b128 v[184:187], v233 offset:36864
	ds_read_b128 v[188:191], v233 offset:37888
	ds_read_b128 v[192:195], v233 offset:38912
	ds_read_b128 v[196:199], v233 offset:39936
	global_load_lds_dwordx4 v[218:219], off nt
	v_lshl_add_u64 v[218:219], s[4:5], 0, v[206:207]
	s_mov_b32 m0, s58
	s_nop 0
	global_load_lds_dwordx4 v[218:219], off nt
	s_waitcnt vmcnt(8)
	s_waitcnt lgkmcnt(0)
	s_barrier
	s_setprio 1
	v_mfma_f32_16x16x32_bf16 v[140:143], v[120:123], v[168:171], v[140:143]
	v_mfma_f32_16x16x32_bf16 v[136:139], v[144:147], v[168:171], v[136:139]
	v_mfma_f32_16x16x32_bf16 v[116:119], v[120:123], v[176:179], v[116:119]
	v_mfma_f32_16x16x32_bf16 v[108:111], v[144:147], v[176:179], v[108:111]
	v_mfma_f32_16x16x32_bf16 v[96:99], v[120:123], v[184:187], v[96:99]
	v_mfma_f32_16x16x32_bf16 v[92:95], v[144:147], v[184:187], v[92:95]
	v_mfma_f32_16x16x32_bf16 v[80:83], v[120:123], v[192:195], v[80:83]
	v_mfma_f32_16x16x32_bf16 v[76:79], v[144:147], v[192:195], v[76:79]
	v_mfma_f32_16x16x32_bf16 v[140:143], v[132:135], v[172:175], v[140:143]
	v_mfma_f32_16x16x32_bf16 v[136:139], v[148:151], v[172:175], v[136:139]
	v_mfma_f32_16x16x32_bf16 v[116:119], v[132:135], v[180:183], v[116:119]
	v_mfma_f32_16x16x32_bf16 v[108:111], v[148:151], v[180:183], v[108:111]
	v_mfma_f32_16x16x32_bf16 v[96:99], v[132:135], v[188:191], v[96:99]
	v_mfma_f32_16x16x32_bf16 v[92:95], v[148:151], v[188:191], v[92:95]
	v_mfma_f32_16x16x32_bf16 v[80:83], v[132:135], v[196:199], v[80:83]
	v_mfma_f32_16x16x32_bf16 v[76:79], v[148:151], v[196:199], v[76:79]
	v_mfma_f32_16x16x32_bf16 v[128:131], v[152:155], v[168:171], v[128:131]
	v_mfma_f32_16x16x32_bf16 v[124:127], v[160:163], v[168:171], v[124:127]
	v_mfma_f32_16x16x32_bf16 v[104:107], v[152:155], v[176:179], v[104:107]
	v_mfma_f32_16x16x32_bf16 v[100:103], v[160:163], v[176:179], v[100:103]
	v_mfma_f32_16x16x32_bf16 v[88:91], v[152:155], v[184:187], v[88:91]
	v_mfma_f32_16x16x32_bf16 v[84:87], v[160:163], v[184:187], v[84:87]
	v_mfma_f32_16x16x32_bf16 v[72:75], v[152:155], v[192:195], v[72:75]
	v_mfma_f32_16x16x32_bf16 v[68:71], v[160:163], v[192:195], v[68:71]
	v_mfma_f32_16x16x32_bf16 v[128:131], v[156:159], v[172:175], v[128:131]
	v_mfma_f32_16x16x32_bf16 v[124:127], v[164:167], v[172:175], v[124:127]
	v_mfma_f32_16x16x32_bf16 v[104:107], v[156:159], v[180:183], v[104:107]
	v_mfma_f32_16x16x32_bf16 v[100:103], v[164:167], v[180:183], v[100:103]
	v_mfma_f32_16x16x32_bf16 v[88:91], v[156:159], v[188:191], v[88:91]
	v_mfma_f32_16x16x32_bf16 v[84:87], v[164:167], v[188:191], v[84:87]
	v_mfma_f32_16x16x32_bf16 v[72:75], v[156:159], v[196:199], v[72:75]
	v_mfma_f32_16x16x32_bf16 v[68:71], v[164:167], v[196:199], v[68:71]
	s_setprio 0
	s_barrier
	s_add_i32 s4, s75, s16
	v_lshl_add_u64 v[214:215], v[214:215], 0, s[34:35]
	s_mov_b32 m0, s4
	ds_read_b128 v[168:171], v233 offset:49152
	ds_read_b128 v[172:175], v233 offset:50176
	ds_read_b128 v[176:179], v233 offset:51200
	ds_read_b128 v[180:183], v233 offset:52224
	ds_read_b128 v[184:187], v233 offset:53248
	ds_read_b128 v[188:191], v233 offset:54272
	ds_read_b128 v[192:195], v233 offset:55296
	ds_read_b128 v[196:199], v233 offset:56320
	global_load_lds_dwordx4 v[214:215], off
	s_add_i32 m0, s4, 0x2000
	s_add_u32 s4, s52, 0x100080
	v_lshl_add_u64 v[214:215], v[216:217], 0, s[34:35]
	s_addc_u32 s5, s53, 0
	s_add_i32 s52, s76, s16
	global_load_lds_dwordx4 v[214:215], off
	v_lshl_add_u64 v[214:215], s[4:5], 0, v[2:3]
	s_mov_b32 m0, s52
	s_nop 0
	global_load_lds_dwordx4 v[214:215], off
	v_lshl_add_u64 v[214:215], s[4:5], 0, v[204:205]
	s_add_i32 m0, s52, 0x2000
	s_nop 0
	global_load_lds_dwordx4 v[214:215], off
	v_lshl_add_u64 v[214:215], s[12:13], 0, v[208:209]
	s_mov_b32 m0, s62
	s_nop 0
	global_load_lds_dwordx4 v[214:215], off nt
	v_lshl_add_u64 v[214:215], s[12:13], 0, v[206:207]
	s_mov_b32 m0, s63
	s_nop 0
	global_load_lds_dwordx4 v[214:215], off nt
	s_waitcnt vmcnt(8)
	s_waitcnt lgkmcnt(0)
	s_barrier
	s_setprio 1
	v_mfma_f32_16x16x32_bf16 v[64:67], v[120:123], v[168:171], v[64:67]
	v_mfma_f32_16x16x32_bf16 v[60:63], v[144:147], v[168:171], v[60:63]
	v_mfma_f32_16x16x32_bf16 v[48:51], v[120:123], v[176:179], v[48:51]
	v_mfma_f32_16x16x32_bf16 v[44:47], v[144:147], v[176:179], v[44:47]
	v_mfma_f32_16x16x32_bf16 v[32:35], v[120:123], v[184:187], v[32:35]
	v_mfma_f32_16x16x32_bf16 v[28:31], v[144:147], v[184:187], v[28:31]
	v_mfma_f32_16x16x32_bf16 v[16:19], v[120:123], v[192:195], v[16:19]
	v_mfma_f32_16x16x32_bf16 v[12:15], v[144:147], v[192:195], v[12:15]
	v_mfma_f32_16x16x32_bf16 v[64:67], v[132:135], v[172:175], v[64:67]
	v_mfma_f32_16x16x32_bf16 v[60:63], v[148:151], v[172:175], v[60:63]
	v_mfma_f32_16x16x32_bf16 v[48:51], v[132:135], v[180:183], v[48:51]
	v_mfma_f32_16x16x32_bf16 v[44:47], v[148:151], v[180:183], v[44:47]
	v_mfma_f32_16x16x32_bf16 v[32:35], v[132:135], v[188:191], v[32:35]
	v_mfma_f32_16x16x32_bf16 v[28:31], v[148:151], v[188:191], v[28:31]
	v_mfma_f32_16x16x32_bf16 v[16:19], v[132:135], v[196:199], v[16:19]
	v_mfma_f32_16x16x32_bf16 v[12:15], v[148:151], v[196:199], v[12:15]
	v_mfma_f32_16x16x32_bf16 v[56:59], v[152:155], v[168:171], v[56:59]
	v_mfma_f32_16x16x32_bf16 v[52:55], v[160:163], v[168:171], v[52:55]
	v_mfma_f32_16x16x32_bf16 v[40:43], v[152:155], v[176:179], v[40:43]
	v_mfma_f32_16x16x32_bf16 v[36:39], v[160:163], v[176:179], v[36:39]
	v_mfma_f32_16x16x32_bf16 v[24:27], v[152:155], v[184:187], v[24:27]
	v_mfma_f32_16x16x32_bf16 v[20:23], v[160:163], v[184:187], v[20:23]
	v_mfma_f32_16x16x32_bf16 v[8:11], v[152:155], v[192:195], v[8:11]
	v_mfma_f32_16x16x32_bf16 v[4:7], v[160:163], v[192:195], v[4:7]
	v_mfma_f32_16x16x32_bf16 v[56:59], v[156:159], v[172:175], v[56:59]
	v_mfma_f32_16x16x32_bf16 v[52:55], v[164:167], v[172:175], v[52:55]
	v_mfma_f32_16x16x32_bf16 v[40:43], v[156:159], v[180:183], v[40:43]
	v_mfma_f32_16x16x32_bf16 v[36:39], v[164:167], v[180:183], v[36:39]
	v_mfma_f32_16x16x32_bf16 v[24:27], v[156:159], v[188:191], v[24:27]
	v_mfma_f32_16x16x32_bf16 v[20:23], v[164:167], v[188:191], v[20:23]
	v_mfma_f32_16x16x32_bf16 v[8:11], v[156:159], v[196:199], v[8:11]
	v_mfma_f32_16x16x32_bf16 v[4:7], v[164:167], v[196:199], v[4:7]
	s_setprio 0
	s_barrier
	s_add_i32 s74, s74, 2
	s_add_u32 s50, s50, 0x100
	s_addc_u32 s51, s51, 0
	s_cmp_gt_u32 s74, 61
.LBB0_1459:
	s_add_u32 s4, s48, s50
	s_addc_u32 s5, s49, s51
	s_add_u32 s75, s4, 0x100
	s_addc_u32 s76, s5, 0
	s_add_u32 s52, s72, s50
	s_addc_u32 s53, s73, s51
	s_add_u32 s4, s4, 0x180
	s_addc_u32 s5, s5, 0
	s_add_i32 s77, 0, 0x10000
	s_add_i32 s78, 0, 0x14000
	v_add_u32_e32 v148, s77, v203
	v_add_u32_e32 v164, s78, v203
	ds_read_b128 v[120:123], v148
	ds_read_b128 v[132:135], v148 offset:1024
	ds_read_b128 v[144:147], v148 offset:2048
	ds_read_b128 v[148:151], v148 offset:3072
	ds_read_b128 v[152:155], v164
	ds_read_b128 v[156:159], v164 offset:1024
	ds_read_b128 v[160:163], v164 offset:2048
	ds_read_b128 v[164:167], v164 offset:3072
	s_cmpk_eq_i32 s50, 0x1f00
	s_cselect_b32 s13, s71, s5
	s_cselect_b32 s12, s70, s4
	s_cselect_b32 s53, s37, s53
	s_cselect_b32 s52, s69, s52
	s_cselect_b32 s5, s41, s76
	s_cselect_b32 s4, s68, s75
	v_lshl_add_u64 v[214:215], v[112:113], 0, s[50:51]
	s_add_i32 m0, s17, 0xc000
	ds_read_b128 v[168:171], v233
	ds_read_b128 v[172:175], v233 offset:1024
	ds_read_b128 v[176:179], v233 offset:2048
	ds_read_b128 v[180:183], v233 offset:3072
	ds_read_b128 v[184:187], v233 offset:4096
	ds_read_b128 v[188:191], v233 offset:5120
	ds_read_b128 v[192:195], v233 offset:6144
	ds_read_b128 v[196:199], v233 offset:7168
	global_load_lds_dwordx4 v[214:215], off nt
	v_lshl_add_u64 v[214:215], v[114:115], 0, s[50:51]
	s_add_i32 m0, s17, 0xe000
	s_nop 0
	global_load_lds_dwordx4 v[214:215], off nt
	s_waitcnt vmcnt(8)
	s_waitcnt lgkmcnt(0)
	s_barrier
	s_setprio 1
	v_mfma_f32_16x16x32_bf16 v[140:143], v[120:123], v[168:171], v[140:143]
	v_mfma_f32_16x16x32_bf16 v[136:139], v[144:147], v[168:171], v[136:139]
	v_mfma_f32_16x16x32_bf16 v[116:119], v[120:123], v[176:179], v[116:119]
	v_mfma_f32_16x16x32_bf16 v[108:111], v[144:147], v[176:179], v[108:111]
	v_mfma_f32_16x16x32_bf16 v[96:99], v[120:123], v[184:187], v[96:99]
	v_mfma_f32_16x16x32_bf16 v[92:95], v[144:147], v[184:187], v[92:95]
	v_mfma_f32_16x16x32_bf16 v[80:83], v[120:123], v[192:195], v[80:83]
	v_mfma_f32_16x16x32_bf16 v[76:79], v[144:147], v[192:195], v[76:79]
	v_mfma_f32_16x16x32_bf16 v[140:143], v[132:135], v[172:175], v[140:143]
	v_mfma_f32_16x16x32_bf16 v[136:139], v[148:151], v[172:175], v[136:139]
	v_mfma_f32_16x16x32_bf16 v[116:119], v[132:135], v[180:183], v[116:119]
	v_mfma_f32_16x16x32_bf16 v[108:111], v[148:151], v[180:183], v[108:111]
	v_mfma_f32_16x16x32_bf16 v[96:99], v[132:135], v[188:191], v[96:99]
	v_mfma_f32_16x16x32_bf16 v[92:95], v[148:151], v[188:191], v[92:95]
	v_mfma_f32_16x16x32_bf16 v[80:83], v[132:135], v[196:199], v[80:83]
	v_mfma_f32_16x16x32_bf16 v[76:79], v[148:151], v[196:199], v[76:79]
	v_mfma_f32_16x16x32_bf16 v[128:131], v[152:155], v[168:171], v[128:131]
	v_mfma_f32_16x16x32_bf16 v[124:127], v[160:163], v[168:171], v[124:127]
	v_mfma_f32_16x16x32_bf16 v[104:107], v[152:155], v[176:179], v[104:107]
	v_mfma_f32_16x16x32_bf16 v[100:103], v[160:163], v[176:179], v[100:103]
	v_mfma_f32_16x16x32_bf16 v[88:91], v[152:155], v[184:187], v[88:91]
	v_mfma_f32_16x16x32_bf16 v[84:87], v[160:163], v[184:187], v[84:87]
	v_mfma_f32_16x16x32_bf16 v[72:75], v[152:155], v[192:195], v[72:75]
	v_mfma_f32_16x16x32_bf16 v[68:71], v[160:163], v[192:195], v[68:71]
	v_mfma_f32_16x16x32_bf16 v[128:131], v[156:159], v[172:175], v[128:131]
	v_mfma_f32_16x16x32_bf16 v[124:127], v[164:167], v[172:175], v[124:127]
	v_mfma_f32_16x16x32_bf16 v[104:107], v[156:159], v[180:183], v[104:107]
	v_mfma_f32_16x16x32_bf16 v[100:103], v[164:167], v[180:183], v[100:103]
	v_mfma_f32_16x16x32_bf16 v[88:91], v[156:159], v[188:191], v[88:91]
	v_mfma_f32_16x16x32_bf16 v[84:87], v[164:167], v[188:191], v[84:87]
	v_mfma_f32_16x16x32_bf16 v[72:75], v[156:159], v[196:199], v[72:75]
	v_mfma_f32_16x16x32_bf16 v[68:71], v[164:167], v[196:199], v[68:71]
	s_setprio 0
	s_barrier
	s_add_i32 s75, s77, s16
	v_lshl_add_u64 v[214:215], s[52:53], 0, v[2:3]
	s_mov_b32 m0, s75
	ds_read_b128 v[168:171], v233 offset:16384
	ds_read_b128 v[172:175], v233 offset:17408
	ds_read_b128 v[176:179], v233 offset:18432
	ds_read_b128 v[180:183], v233 offset:19456
	ds_read_b128 v[184:187], v233 offset:20480
	ds_read_b128 v[188:191], v233 offset:21504
	ds_read_b128 v[192:195], v233 offset:22528
	ds_read_b128 v[196:199], v233 offset:23552
	global_load_lds_dwordx4 v[214:215], off
	s_add_i32 m0, s75, 0x2000
	s_add_u32 s76, s52, 0x100000
	v_lshl_add_u64 v[216:217], s[52:53], 0, v[204:205]
	s_addc_u32 s77, s53, 0
	s_add_i32 s75, s78, s16
	global_load_lds_dwordx4 v[216:217], off
	v_lshl_add_u64 v[218:219], s[76:77], 0, v[2:3]
	s_mov_b32 m0, s75
	s_nop 0
	global_load_lds_dwordx4 v[218:219], off
	v_lshl_add_u64 v[218:219], s[76:77], 0, v[204:205]
	s_add_i32 m0, s75, 0x2000
	s_nop 0
	global_load_lds_dwordx4 v[218:219], off
	v_lshl_add_u64 v[218:219], s[4:5], 0, v[208:209]
	s_mov_b32 m0, s17
	s_nop 0
	global_load_lds_dwordx4 v[218:219], off nt
	v_lshl_add_u64 v[218:219], s[4:5], 0, v[206:207]
	s_mov_b32 m0, s46
	s_nop 0
	global_load_lds_dwordx4 v[218:219], off nt
	s_waitcnt vmcnt(8)
	s_waitcnt lgkmcnt(0)
	s_barrier
	s_setprio 1
	v_mfma_f32_16x16x32_bf16 v[64:67], v[120:123], v[168:171], v[64:67]
	v_mfma_f32_16x16x32_bf16 v[60:63], v[144:147], v[168:171], v[60:63]
	v_mfma_f32_16x16x32_bf16 v[48:51], v[120:123], v[176:179], v[48:51]
	v_mfma_f32_16x16x32_bf16 v[44:47], v[144:147], v[176:179], v[44:47]
	v_mfma_f32_16x16x32_bf16 v[32:35], v[120:123], v[184:187], v[32:35]
	v_mfma_f32_16x16x32_bf16 v[28:31], v[144:147], v[184:187], v[28:31]
	v_mfma_f32_16x16x32_bf16 v[16:19], v[120:123], v[192:195], v[16:19]
	v_mfma_f32_16x16x32_bf16 v[12:15], v[144:147], v[192:195], v[12:15]
	v_mfma_f32_16x16x32_bf16 v[64:67], v[132:135], v[172:175], v[64:67]
	v_mfma_f32_16x16x32_bf16 v[60:63], v[148:151], v[172:175], v[60:63]
	v_mfma_f32_16x16x32_bf16 v[48:51], v[132:135], v[180:183], v[48:51]
	v_mfma_f32_16x16x32_bf16 v[44:47], v[148:151], v[180:183], v[44:47]
	v_mfma_f32_16x16x32_bf16 v[32:35], v[132:135], v[188:191], v[32:35]
	v_mfma_f32_16x16x32_bf16 v[28:31], v[148:151], v[188:191], v[28:31]
	v_mfma_f32_16x16x32_bf16 v[16:19], v[132:135], v[196:199], v[16:19]
	v_mfma_f32_16x16x32_bf16 v[12:15], v[148:151], v[196:199], v[12:15]
	v_mfma_f32_16x16x32_bf16 v[56:59], v[152:155], v[168:171], v[56:59]
	v_mfma_f32_16x16x32_bf16 v[52:55], v[160:163], v[168:171], v[52:55]
	v_mfma_f32_16x16x32_bf16 v[40:43], v[152:155], v[176:179], v[40:43]
	v_mfma_f32_16x16x32_bf16 v[36:39], v[160:163], v[176:179], v[36:39]
	v_mfma_f32_16x16x32_bf16 v[24:27], v[152:155], v[184:187], v[24:27]
	v_mfma_f32_16x16x32_bf16 v[20:23], v[160:163], v[184:187], v[20:23]
	v_mfma_f32_16x16x32_bf16 v[8:11], v[152:155], v[192:195], v[8:11]
	v_mfma_f32_16x16x32_bf16 v[4:7], v[160:163], v[192:195], v[4:7]
	v_mfma_f32_16x16x32_bf16 v[56:59], v[156:159], v[172:175], v[56:59]
	v_mfma_f32_16x16x32_bf16 v[52:55], v[164:167], v[172:175], v[52:55]
	v_mfma_f32_16x16x32_bf16 v[40:43], v[156:159], v[180:183], v[40:43]
	v_mfma_f32_16x16x32_bf16 v[36:39], v[164:167], v[180:183], v[36:39]
	v_mfma_f32_16x16x32_bf16 v[24:27], v[156:159], v[188:191], v[24:27]
	v_mfma_f32_16x16x32_bf16 v[20:23], v[164:167], v[188:191], v[20:23]
	v_mfma_f32_16x16x32_bf16 v[8:11], v[156:159], v[196:199], v[8:11]
	v_mfma_f32_16x16x32_bf16 v[4:7], v[164:167], v[196:199], v[4:7]
	s_setprio 0
	s_barrier
	s_add_i32 s75, 0, 0x18000
	s_add_i32 s76, 0, 0x1c000
	v_add_u32_e32 v148, s75, v203
	v_add_u32_e32 v164, s76, v203
	ds_read_b128 v[120:123], v148
	ds_read_b128 v[132:135], v148 offset:1024
	ds_read_b128 v[144:147], v148 offset:2048
	ds_read_b128 v[148:151], v148 offset:3072
	ds_read_b128 v[152:155], v164
	ds_read_b128 v[156:159], v164 offset:1024
	ds_read_b128 v[160:163], v164 offset:2048
	ds_read_b128 v[164:167], v164 offset:3072
	s_add_u32 s4, s4, 0x100000
	s_addc_u32 s5, s5, 0
	s_mov_b32 m0, s47
	v_lshl_add_u64 v[218:219], s[4:5], 0, v[208:209]
	ds_read_b128 v[168:171], v233 offset:32768
	ds_read_b128 v[172:175], v233 offset:33792
	ds_read_b128 v[176:179], v233 offset:34816
	ds_read_b128 v[180:183], v233 offset:35840
	ds_read_b128 v[184:187], v233 offset:36864
	ds_read_b128 v[188:191], v233 offset:37888
	ds_read_b128 v[192:195], v233 offset:38912
	ds_read_b128 v[196:199], v233 offset:39936
	global_load_lds_dwordx4 v[218:219], off nt
	v_lshl_add_u64 v[218:219], s[4:5], 0, v[206:207]
	s_mov_b32 m0, s58
	s_nop 0
	global_load_lds_dwordx4 v[218:219], off nt
	s_waitcnt vmcnt(8)
	s_waitcnt lgkmcnt(0)
	s_barrier
	s_setprio 1
	v_mfma_f32_16x16x32_bf16 v[140:143], v[120:123], v[168:171], v[140:143]
	v_mfma_f32_16x16x32_bf16 v[136:139], v[144:147], v[168:171], v[136:139]
	v_mfma_f32_16x16x32_bf16 v[116:119], v[120:123], v[176:179], v[116:119]
	v_mfma_f32_16x16x32_bf16 v[108:111], v[144:147], v[176:179], v[108:111]
	v_mfma_f32_16x16x32_bf16 v[96:99], v[120:123], v[184:187], v[96:99]
	v_mfma_f32_16x16x32_bf16 v[92:95], v[144:147], v[184:187], v[92:95]
	v_mfma_f32_16x16x32_bf16 v[80:83], v[120:123], v[192:195], v[80:83]
	v_mfma_f32_16x16x32_bf16 v[76:79], v[144:147], v[192:195], v[76:79]
	v_mfma_f32_16x16x32_bf16 v[140:143], v[132:135], v[172:175], v[140:143]
	v_mfma_f32_16x16x32_bf16 v[136:139], v[148:151], v[172:175], v[136:139]
	v_mfma_f32_16x16x32_bf16 v[116:119], v[132:135], v[180:183], v[116:119]
	v_mfma_f32_16x16x32_bf16 v[108:111], v[148:151], v[180:183], v[108:111]
	v_mfma_f32_16x16x32_bf16 v[96:99], v[132:135], v[188:191], v[96:99]
	v_mfma_f32_16x16x32_bf16 v[92:95], v[148:151], v[188:191], v[92:95]
	v_mfma_f32_16x16x32_bf16 v[80:83], v[132:135], v[196:199], v[80:83]
	v_mfma_f32_16x16x32_bf16 v[76:79], v[148:151], v[196:199], v[76:79]
	v_mfma_f32_16x16x32_bf16 v[128:131], v[152:155], v[168:171], v[128:131]
	v_mfma_f32_16x16x32_bf16 v[124:127], v[160:163], v[168:171], v[124:127]
	v_mfma_f32_16x16x32_bf16 v[104:107], v[152:155], v[176:179], v[104:107]
	v_mfma_f32_16x16x32_bf16 v[100:103], v[160:163], v[176:179], v[100:103]
	v_mfma_f32_16x16x32_bf16 v[88:91], v[152:155], v[184:187], v[88:91]
	v_mfma_f32_16x16x32_bf16 v[84:87], v[160:163], v[184:187], v[84:87]
	v_mfma_f32_16x16x32_bf16 v[72:75], v[152:155], v[192:195], v[72:75]
	v_mfma_f32_16x16x32_bf16 v[68:71], v[160:163], v[192:195], v[68:71]
	v_mfma_f32_16x16x32_bf16 v[128:131], v[156:159], v[172:175], v[128:131]
	v_mfma_f32_16x16x32_bf16 v[124:127], v[164:167], v[172:175], v[124:127]
	v_mfma_f32_16x16x32_bf16 v[104:107], v[156:159], v[180:183], v[104:107]
	v_mfma_f32_16x16x32_bf16 v[100:103], v[164:167], v[180:183], v[100:103]
	v_mfma_f32_16x16x32_bf16 v[88:91], v[156:159], v[188:191], v[88:91]
	v_mfma_f32_16x16x32_bf16 v[84:87], v[164:167], v[188:191], v[84:87]
	v_mfma_f32_16x16x32_bf16 v[72:75], v[156:159], v[196:199], v[72:75]
	v_mfma_f32_16x16x32_bf16 v[68:71], v[164:167], v[196:199], v[68:71]
	s_setprio 0
	s_barrier
	s_add_i32 s4, s75, s16
	v_lshl_add_u64 v[214:215], v[214:215], 0, s[34:35]
	s_mov_b32 m0, s4
	ds_read_b128 v[168:171], v233 offset:49152
	ds_read_b128 v[172:175], v233 offset:50176
	ds_read_b128 v[176:179], v233 offset:51200
	ds_read_b128 v[180:183], v233 offset:52224
	ds_read_b128 v[184:187], v233 offset:53248
	ds_read_b128 v[188:191], v233 offset:54272
	ds_read_b128 v[192:195], v233 offset:55296
	ds_read_b128 v[196:199], v233 offset:56320
	global_load_lds_dwordx4 v[214:215], off
	s_add_i32 m0, s4, 0x2000
	s_add_u32 s4, s52, 0x100080
	v_lshl_add_u64 v[214:215], v[216:217], 0, s[34:35]
	s_addc_u32 s5, s53, 0
	s_add_i32 s52, s76, s16
	global_load_lds_dwordx4 v[214:215], off
	v_lshl_add_u64 v[214:215], s[4:5], 0, v[2:3]
	s_mov_b32 m0, s52
	s_nop 0
	global_load_lds_dwordx4 v[214:215], off
	v_lshl_add_u64 v[214:215], s[4:5], 0, v[204:205]
	s_add_i32 m0, s52, 0x2000
	s_nop 0
	global_load_lds_dwordx4 v[214:215], off
	v_lshl_add_u64 v[214:215], s[12:13], 0, v[208:209]
	s_mov_b32 m0, s62
	s_nop 0
	global_load_lds_dwordx4 v[214:215], off nt
	v_lshl_add_u64 v[214:215], s[12:13], 0, v[206:207]
	s_mov_b32 m0, s63
	s_nop 0
	global_load_lds_dwordx4 v[214:215], off nt
	s_waitcnt vmcnt(8)
	s_waitcnt lgkmcnt(0)
	s_barrier
	s_setprio 1
	v_mfma_f32_16x16x32_bf16 v[64:67], v[120:123], v[168:171], v[64:67]
	v_mfma_f32_16x16x32_bf16 v[60:63], v[144:147], v[168:171], v[60:63]
	v_mfma_f32_16x16x32_bf16 v[48:51], v[120:123], v[176:179], v[48:51]
	v_mfma_f32_16x16x32_bf16 v[44:47], v[144:147], v[176:179], v[44:47]
	v_mfma_f32_16x16x32_bf16 v[32:35], v[120:123], v[184:187], v[32:35]
	v_mfma_f32_16x16x32_bf16 v[28:31], v[144:147], v[184:187], v[28:31]
	v_mfma_f32_16x16x32_bf16 v[16:19], v[120:123], v[192:195], v[16:19]
	v_mfma_f32_16x16x32_bf16 v[12:15], v[144:147], v[192:195], v[12:15]
	v_mfma_f32_16x16x32_bf16 v[64:67], v[132:135], v[172:175], v[64:67]
	v_mfma_f32_16x16x32_bf16 v[60:63], v[148:151], v[172:175], v[60:63]
	v_mfma_f32_16x16x32_bf16 v[48:51], v[132:135], v[180:183], v[48:51]
	v_mfma_f32_16x16x32_bf16 v[44:47], v[148:151], v[180:183], v[44:47]
	v_mfma_f32_16x16x32_bf16 v[32:35], v[132:135], v[188:191], v[32:35]
	v_mfma_f32_16x16x32_bf16 v[28:31], v[148:151], v[188:191], v[28:31]
	v_mfma_f32_16x16x32_bf16 v[16:19], v[132:135], v[196:199], v[16:19]
	v_mfma_f32_16x16x32_bf16 v[12:15], v[148:151], v[196:199], v[12:15]
	v_mfma_f32_16x16x32_bf16 v[56:59], v[152:155], v[168:171], v[56:59]
	v_mfma_f32_16x16x32_bf16 v[52:55], v[160:163], v[168:171], v[52:55]
	v_mfma_f32_16x16x32_bf16 v[40:43], v[152:155], v[176:179], v[40:43]
	v_mfma_f32_16x16x32_bf16 v[36:39], v[160:163], v[176:179], v[36:39]
	v_mfma_f32_16x16x32_bf16 v[24:27], v[152:155], v[184:187], v[24:27]
	v_mfma_f32_16x16x32_bf16 v[20:23], v[160:163], v[184:187], v[20:23]
	v_mfma_f32_16x16x32_bf16 v[8:11], v[152:155], v[192:195], v[8:11]
	v_mfma_f32_16x16x32_bf16 v[4:7], v[160:163], v[192:195], v[4:7]
	v_mfma_f32_16x16x32_bf16 v[56:59], v[156:159], v[172:175], v[56:59]
	v_mfma_f32_16x16x32_bf16 v[52:55], v[164:167], v[172:175], v[52:55]
	v_mfma_f32_16x16x32_bf16 v[40:43], v[156:159], v[180:183], v[40:43]
	v_mfma_f32_16x16x32_bf16 v[36:39], v[164:167], v[180:183], v[36:39]
	v_mfma_f32_16x16x32_bf16 v[24:27], v[156:159], v[188:191], v[24:27]
	v_mfma_f32_16x16x32_bf16 v[20:23], v[164:167], v[188:191], v[20:23]
	v_mfma_f32_16x16x32_bf16 v[8:11], v[156:159], v[196:199], v[8:11]
	v_mfma_f32_16x16x32_bf16 v[4:7], v[164:167], v[196:199], v[4:7]
	s_setprio 0
	s_barrier
	s_add_i32 s74, s74, 2
	s_add_u32 s50, s50, 0x100
	s_addc_u32 s51, s51, 0
	s_cmp_gt_u32 s74, 61
	s_cbranch_scc0 .LBB0_1459
	s_and_b64 vcc, exec, s[22:23]
	s_cbranch_vccz .LBB0_1462
	s_barrier
